# v50 + NSA selected-branch P.V phase rescheduled MFMA-first: k-steps 0,1 of all four output tiles issue first with the second S-tile's exp and row-sum VALU spread under them; same per-accumulator order
# baseline (speedup 1.0000x reference)
.LBB0_1748:
	ds_read_b64_tr_b16 v[196:197], v0 offset:0
	ds_read_b64_tr_b16 v[198:199], v0 offset:0x800
	ds_read_b64_tr_b16 v[200:201], v0 offset:0x1000
	ds_read_b64_tr_b16 v[202:203], v0 offset:0x1800
	ds_read_b64_tr_b16 v[204:205], v0 offset:0x200
	ds_read_b64_tr_b16 v[206:207], v0 offset:0xa00
	ds_read_b64_tr_b16 v[208:209], v0 offset:0x1200
	ds_read_b64_tr_b16 v[210:211], v0 offset:0x1a00
	v_cvt_pk_bf16_f32 v180, v68, v69
	v_cvt_pk_bf16_f32 v181, v70, v71
	v_cvt_pk_bf16_f32 v182, v72, v73
	v_cvt_pk_bf16_f32 v183, v74, v75
	v_cvt_pk_bf16_f32 v184, v76, v77
	v_cvt_pk_bf16_f32 v185, v78, v79
	v_cvt_pk_bf16_f32 v186, v80, v81
	v_cvt_pk_bf16_f32 v187, v82, v83
	v_permlane32_swap_b32_e32 v180, v182
	v_permlane32_swap_b32_e32 v181, v183
	v_permlane32_swap_b32_e32 v184, v186
	v_permlane32_swap_b32_e32 v185, v187
	v_exp_f32_e32 v84, v84
	v_exp_f32_e32 v85, v85
	v_exp_f32_e32 v86, v86
	v_exp_f32_e32 v87, v87
	v_exp_f32_e32 v88, v88
	v_exp_f32_e32 v89, v89
	s_waitcnt lgkmcnt(4)
	v_mfma_f32_32x32x16_bf16 v[20:35], v[180:183], v[196:199], v[20:35]
	v_mfma_f32_32x32x16_bf16 v[20:35], v[184:187], v[200:203], v[20:35]
	ds_read_b64_tr_b16 v[196:197], v0 offset:0x400
	ds_read_b64_tr_b16 v[198:199], v0 offset:0xc00
	ds_read_b64_tr_b16 v[200:201], v0 offset:0x1400
	ds_read_b64_tr_b16 v[202:203], v0 offset:0x1c00
	v_exp_f32_e32 v90, v90
	v_exp_f32_e32 v91, v91
	v_exp_f32_e32 v92, v92
	v_exp_f32_e32 v93, v93
	v_add_f32_e32 v226, v68, v84
	v_add_f32_e32 v227, v69, v85
	v_exp_f32_e32 v94, v94
	v_exp_f32_e32 v95, v95
	v_add_f32_e32 v224, v70, v86
	v_add_f32_e32 v225, v71, v87
	v_add_f32_e32 v226, 0, v226
	v_add_f32_e32 v227, 0, v227
	s_waitcnt lgkmcnt(4)
	v_mfma_f32_32x32x16_bf16 v[36:51], v[180:183], v[204:207], v[36:51]
	v_mfma_f32_32x32x16_bf16 v[36:51], v[184:187], v[208:211], v[36:51]
	ds_read_b64_tr_b16 v[204:205], v0 offset:0x600
	ds_read_b64_tr_b16 v[206:207], v0 offset:0xe00
	ds_read_b64_tr_b16 v[208:209], v0 offset:0x1600
	ds_read_b64_tr_b16 v[210:211], v0 offset:0x1e00
	v_exp_f32_e32 v96, v96
	v_exp_f32_e32 v97, v97
	v_add_f32_e32 v222, v72, v88
	v_add_f32_e32 v223, v73, v89
	v_add_f32_e32 v224, v224, v226
	v_add_f32_e32 v225, v225, v227
	v_exp_f32_e32 v98, v98
	v_exp_f32_e32 v99, v99
	v_add_f32_e32 v220, v74, v90
	v_add_f32_e32 v221, v75, v91
	v_add_f32_e32 v222, v222, v224
	v_add_f32_e32 v223, v223, v225
	s_waitcnt lgkmcnt(4)
	v_mfma_f32_32x32x16_bf16 v[52:67], v[180:183], v[196:199], v[52:67]
	v_mfma_f32_32x32x16_bf16 v[52:67], v[184:187], v[200:203], v[52:67]
	ds_read_b64_tr_b16 v[196:197], v0 offset:0x2000
	ds_read_b64_tr_b16 v[198:199], v0 offset:0x2800
	ds_read_b64_tr_b16 v[200:201], v0 offset:0x3000
	ds_read_b64_tr_b16 v[202:203], v0 offset:0x3800
	v_add_f32_e32 v218, v76, v92
	v_add_f32_e32 v219, v77, v93
	v_add_f32_e32 v220, v220, v222
	v_add_f32_e32 v221, v221, v223
	v_add_f32_e32 v216, v78, v94
	v_add_f32_e32 v217, v79, v95
	v_add_f32_e32 v218, v218, v220
	v_add_f32_e32 v219, v219, v221
	v_add_f32_e32 v214, v80, v96
	v_add_f32_e32 v215, v81, v97
	v_add_f32_e32 v216, v216, v218
	v_add_f32_e32 v217, v217, v219
	s_waitcnt lgkmcnt(4)
	v_mfma_f32_32x32x16_bf16 v[4:19], v[180:183], v[204:207], v[4:19]
	v_mfma_f32_32x32x16_bf16 v[4:19], v[184:187], v[208:211], v[4:19]
	ds_read_b64_tr_b16 v[204:205], v0 offset:0x2200
	ds_read_b64_tr_b16 v[206:207], v0 offset:0x2a00
	ds_read_b64_tr_b16 v[208:209], v0 offset:0x3200
	ds_read_b64_tr_b16 v[210:211], v0 offset:0x3a00
	v_add_f32_e32 v212, v82, v98
	v_add_f32_e32 v213, v83, v99
	v_add_f32_e32 v214, v214, v216
	v_add_f32_e32 v215, v215, v217
	s_nop 0
	v_add_f32_e32 v212, v212, v214
	v_add_f32_e32 v213, v213, v215
	s_nop 0
	v_pk_add_f32 v[212:213], v[212:213], v[212:213] op_sel:[0,1] op_sel_hi:[1,0]
	s_nop 0
	v_mov_b32_e32 v1, v212
	s_nop 1
	v_permlane32_swap_b32_e32 v212, v1
	v_add_f32_e32 v1, v212, v1
	v_fmac_f32_e32 v1, v138, v178
	v_mov_b32_e32 v138, v1
	v_cvt_pk_bf16_f32 v188, v84, v85
	v_cvt_pk_bf16_f32 v189, v86, v87
	v_cvt_pk_bf16_f32 v190, v88, v89
	v_cvt_pk_bf16_f32 v191, v90, v91
	v_cvt_pk_bf16_f32 v192, v92, v93
	v_cvt_pk_bf16_f32 v193, v94, v95
	v_cvt_pk_bf16_f32 v194, v96, v97
	v_cvt_pk_bf16_f32 v195, v98, v99
	v_permlane32_swap_b32_e32 v188, v190
	v_permlane32_swap_b32_e32 v189, v191
	v_permlane32_swap_b32_e32 v192, v194
	v_permlane32_swap_b32_e32 v193, v195
	s_nop 1
	s_waitcnt lgkmcnt(4)
	v_mfma_f32_32x32x16_bf16 v[20:35], v[188:191], v[196:199], v[20:35]
	v_mfma_f32_32x32x16_bf16 v[20:35], v[192:195], v[200:203], v[20:35]
	ds_read_b64_tr_b16 v[196:197], v0 offset:0x2400
	ds_read_b64_tr_b16 v[198:199], v0 offset:0x2c00
	ds_read_b64_tr_b16 v[200:201], v0 offset:0x3400
	ds_read_b64_tr_b16 v[202:203], v0 offset:0x3c00
	s_waitcnt lgkmcnt(4)
	v_mfma_f32_32x32x16_bf16 v[36:51], v[188:191], v[204:207], v[36:51]
	v_mfma_f32_32x32x16_bf16 v[36:51], v[192:195], v[208:211], v[36:51]
	ds_read_b64_tr_b16 v[204:205], v0 offset:0x2600
	ds_read_b64_tr_b16 v[206:207], v0 offset:0x2e00
	ds_read_b64_tr_b16 v[208:209], v0 offset:0x3600
	ds_read_b64_tr_b16 v[210:211], v0 offset:0x3e00
	s_waitcnt lgkmcnt(4)
	v_mfma_f32_32x32x16_bf16 v[52:67], v[188:191], v[196:199], v[52:67]
	v_mfma_f32_32x32x16_bf16 v[52:67], v[192:195], v[200:203], v[52:67]
	s_waitcnt lgkmcnt(0)
	v_mfma_f32_32x32x16_bf16 v[4:19], v[188:191], v[204:207], v[4:19]
	v_mfma_f32_32x32x16_bf16 v[4:19], v[192:195], v[208:211], v[4:19]

.LBB0_1776:
	ds_read_b64_tr_b16 v[196:197], v136 offset:0
	ds_read_b64_tr_b16 v[198:199], v136 offset:0x800
	ds_read_b64_tr_b16 v[200:201], v136 offset:0x1000
	ds_read_b64_tr_b16 v[202:203], v136 offset:0x1800
	ds_read_b64_tr_b16 v[204:205], v136 offset:0x200
	ds_read_b64_tr_b16 v[206:207], v136 offset:0xa00
	ds_read_b64_tr_b16 v[208:209], v136 offset:0x1200
	ds_read_b64_tr_b16 v[210:211], v136 offset:0x1a00
	v_cvt_pk_bf16_f32 v180, v68, v69
	v_cvt_pk_bf16_f32 v181, v70, v71
	v_cvt_pk_bf16_f32 v182, v72, v73
	v_cvt_pk_bf16_f32 v183, v74, v75
	v_cvt_pk_bf16_f32 v184, v76, v77
	v_cvt_pk_bf16_f32 v185, v78, v79
	v_cvt_pk_bf16_f32 v186, v80, v81
	v_cvt_pk_bf16_f32 v187, v82, v83
	v_permlane32_swap_b32_e32 v180, v182
	v_permlane32_swap_b32_e32 v181, v183
	v_permlane32_swap_b32_e32 v184, v186
	v_permlane32_swap_b32_e32 v185, v187
	v_exp_f32_e32 v84, v84
	v_exp_f32_e32 v85, v85
	v_exp_f32_e32 v86, v86
	v_exp_f32_e32 v87, v87
	v_exp_f32_e32 v88, v88
	v_exp_f32_e32 v89, v89
	s_waitcnt lgkmcnt(4)
	v_mfma_f32_32x32x16_bf16 v[20:35], v[180:183], v[196:199], v[20:35]
	v_mfma_f32_32x32x16_bf16 v[20:35], v[184:187], v[200:203], v[20:35]
	ds_read_b64_tr_b16 v[196:197], v136 offset:0x400
	ds_read_b64_tr_b16 v[198:199], v136 offset:0xc00
	ds_read_b64_tr_b16 v[200:201], v136 offset:0x1400
	ds_read_b64_tr_b16 v[202:203], v136 offset:0x1c00
	v_exp_f32_e32 v90, v90
	v_exp_f32_e32 v91, v91
	v_exp_f32_e32 v92, v92
	v_exp_f32_e32 v93, v93
	v_add_f32_e32 v226, v68, v84
	v_add_f32_e32 v227, v69, v85
	v_exp_f32_e32 v94, v94
	v_exp_f32_e32 v95, v95
	v_add_f32_e32 v224, v70, v86
	v_add_f32_e32 v225, v71, v87
	v_add_f32_e32 v226, 0, v226
	v_add_f32_e32 v227, 0, v227
	s_waitcnt lgkmcnt(4)
	v_mfma_f32_32x32x16_bf16 v[36:51], v[180:183], v[204:207], v[36:51]
	v_mfma_f32_32x32x16_bf16 v[36:51], v[184:187], v[208:211], v[36:51]
	ds_read_b64_tr_b16 v[204:205], v136 offset:0x600
	ds_read_b64_tr_b16 v[206:207], v136 offset:0xe00
	ds_read_b64_tr_b16 v[208:209], v136 offset:0x1600
	ds_read_b64_tr_b16 v[210:211], v136 offset:0x1e00
	v_exp_f32_e32 v96, v96
	v_exp_f32_e32 v97, v97
	v_add_f32_e32 v222, v72, v88
	v_add_f32_e32 v223, v73, v89
	v_add_f32_e32 v224, v224, v226
	v_add_f32_e32 v225, v225, v227
	v_exp_f32_e32 v98, v98
	v_exp_f32_e32 v99, v99
	v_add_f32_e32 v220, v74, v90
	v_add_f32_e32 v221, v75, v91
	v_add_f32_e32 v222, v222, v224
	v_add_f32_e32 v223, v223, v225
	s_waitcnt lgkmcnt(4)
	v_mfma_f32_32x32x16_bf16 v[52:67], v[180:183], v[196:199], v[52:67]
	v_mfma_f32_32x32x16_bf16 v[52:67], v[184:187], v[200:203], v[52:67]
	ds_read_b64_tr_b16 v[196:197], v136 offset:0x2000
	ds_read_b64_tr_b16 v[198:199], v136 offset:0x2800
	ds_read_b64_tr_b16 v[200:201], v136 offset:0x3000
	ds_read_b64_tr_b16 v[202:203], v136 offset:0x3800
	v_add_f32_e32 v218, v76, v92
	v_add_f32_e32 v219, v77, v93
	v_add_f32_e32 v220, v220, v222
	v_add_f32_e32 v221, v221, v223
	v_add_f32_e32 v216, v78, v94
	v_add_f32_e32 v217, v79, v95
	v_add_f32_e32 v218, v218, v220
	v_add_f32_e32 v219, v219, v221
	v_add_f32_e32 v214, v80, v96
	v_add_f32_e32 v215, v81, v97
	v_add_f32_e32 v216, v216, v218
	v_add_f32_e32 v217, v217, v219
	s_waitcnt lgkmcnt(4)
	v_mfma_f32_32x32x16_bf16 v[4:19], v[180:183], v[204:207], v[4:19]
	v_mfma_f32_32x32x16_bf16 v[4:19], v[184:187], v[208:211], v[4:19]
	ds_read_b64_tr_b16 v[204:205], v136 offset:0x2200
	ds_read_b64_tr_b16 v[206:207], v136 offset:0x2a00
	ds_read_b64_tr_b16 v[208:209], v136 offset:0x3200
	ds_read_b64_tr_b16 v[210:211], v136 offset:0x3a00
	v_add_f32_e32 v212, v82, v98
	v_add_f32_e32 v213, v83, v99
	v_add_f32_e32 v214, v214, v216
	v_add_f32_e32 v215, v215, v217
	s_nop 0
	v_add_f32_e32 v212, v212, v214
	v_add_f32_e32 v213, v213, v215
	s_nop 0
	v_pk_add_f32 v[212:213], v[212:213], v[212:213] op_sel:[0,1] op_sel_hi:[1,0]
	s_nop 0
	v_mov_b32_e32 v1, v212
	s_nop 1
	v_permlane32_swap_b32_e32 v212, v1
	v_add_f32_e32 v1, v212, v1
	v_fmac_f32_e32 v1, v138, v178
	v_mov_b32_e32 v138, v1
	v_cvt_pk_bf16_f32 v188, v84, v85
	v_cvt_pk_bf16_f32 v189, v86, v87
	v_cvt_pk_bf16_f32 v190, v88, v89
	v_cvt_pk_bf16_f32 v191, v90, v91
	v_cvt_pk_bf16_f32 v192, v92, v93
	v_cvt_pk_bf16_f32 v193, v94, v95
	v_cvt_pk_bf16_f32 v194, v96, v97
	v_cvt_pk_bf16_f32 v195, v98, v99
	v_permlane32_swap_b32_e32 v188, v190
	v_permlane32_swap_b32_e32 v189, v191
	v_permlane32_swap_b32_e32 v192, v194
	v_permlane32_swap_b32_e32 v193, v195
	s_nop 1
	s_waitcnt lgkmcnt(4)
	v_mfma_f32_32x32x16_bf16 v[20:35], v[188:191], v[196:199], v[20:35]
	v_mfma_f32_32x32x16_bf16 v[20:35], v[192:195], v[200:203], v[20:35]
	ds_read_b64_tr_b16 v[196:197], v136 offset:0x2400
	ds_read_b64_tr_b16 v[198:199], v136 offset:0x2c00
	ds_read_b64_tr_b16 v[200:201], v136 offset:0x3400
	ds_read_b64_tr_b16 v[202:203], v136 offset:0x3c00
	s_waitcnt lgkmcnt(4)
	v_mfma_f32_32x32x16_bf16 v[36:51], v[188:191], v[204:207], v[36:51]
	v_mfma_f32_32x32x16_bf16 v[36:51], v[192:195], v[208:211], v[36:51]
	ds_read_b64_tr_b16 v[204:205], v136 offset:0x2600
	ds_read_b64_tr_b16 v[206:207], v136 offset:0x2e00
	ds_read_b64_tr_b16 v[208:209], v136 offset:0x3600
	ds_read_b64_tr_b16 v[210:211], v136 offset:0x3e00
	s_waitcnt lgkmcnt(4)
	v_mfma_f32_32x32x16_bf16 v[52:67], v[188:191], v[196:199], v[52:67]
	v_mfma_f32_32x32x16_bf16 v[52:67], v[192:195], v[200:203], v[52:67]
	s_waitcnt lgkmcnt(0)
	v_mfma_f32_32x32x16_bf16 v[4:19], v[188:191], v[204:207], v[4:19]
	v_mfma_f32_32x32x16_bf16 v[4:19], v[192:195], v[208:211], v[4:19]

.LBB0_1843:
	ds_read_b64_tr_b16 v[186:187], v0 offset:0
	ds_read_b64_tr_b16 v[188:189], v0 offset:0x800
	ds_read_b64_tr_b16 v[190:191], v0 offset:0x1000
	ds_read_b64_tr_b16 v[192:193], v0 offset:0x1800
	ds_read_b64_tr_b16 v[194:195], v0 offset:0x200
	ds_read_b64_tr_b16 v[196:197], v0 offset:0xa00
	ds_read_b64_tr_b16 v[198:199], v0 offset:0x1200
	ds_read_b64_tr_b16 v[200:201], v0 offset:0x1a00
	v_cvt_pk_bf16_f32 v170, v68, v69
	v_cvt_pk_bf16_f32 v171, v70, v71
	v_cvt_pk_bf16_f32 v172, v72, v73
	v_cvt_pk_bf16_f32 v173, v74, v75
	v_cvt_pk_bf16_f32 v174, v76, v77
	v_cvt_pk_bf16_f32 v175, v78, v79
	v_cvt_pk_bf16_f32 v176, v80, v81
	v_cvt_pk_bf16_f32 v177, v82, v83
	v_permlane32_swap_b32_e32 v170, v172
	v_permlane32_swap_b32_e32 v171, v173
	v_permlane32_swap_b32_e32 v174, v176
	v_permlane32_swap_b32_e32 v175, v177
	v_exp_f32_e32 v84, v84
	v_exp_f32_e32 v85, v85
	v_exp_f32_e32 v86, v86
	v_exp_f32_e32 v87, v87
	v_exp_f32_e32 v88, v88
	v_exp_f32_e32 v89, v89
	s_waitcnt lgkmcnt(4)
	v_mfma_f32_32x32x16_bf16 v[20:35], v[170:173], v[186:189], v[20:35]
	v_mfma_f32_32x32x16_bf16 v[20:35], v[174:177], v[190:193], v[20:35]
	ds_read_b64_tr_b16 v[186:187], v0 offset:0x400
	ds_read_b64_tr_b16 v[188:189], v0 offset:0xc00
	ds_read_b64_tr_b16 v[190:191], v0 offset:0x1400
	ds_read_b64_tr_b16 v[192:193], v0 offset:0x1c00
	v_exp_f32_e32 v90, v90
	v_exp_f32_e32 v91, v91
	v_exp_f32_e32 v92, v92
	v_exp_f32_e32 v93, v93
	v_add_f32_e32 v226, v68, v84
	v_add_f32_e32 v227, v69, v85
	v_exp_f32_e32 v94, v94
	v_exp_f32_e32 v95, v95
	v_add_f32_e32 v224, v70, v86
	v_add_f32_e32 v225, v71, v87
	v_add_f32_e32 v226, 0, v226
	v_add_f32_e32 v227, 0, v227
	s_waitcnt lgkmcnt(4)
	v_mfma_f32_32x32x16_bf16 v[36:51], v[170:173], v[194:197], v[36:51]
	v_mfma_f32_32x32x16_bf16 v[36:51], v[174:177], v[198:201], v[36:51]
	ds_read_b64_tr_b16 v[194:195], v0 offset:0x600
	ds_read_b64_tr_b16 v[196:197], v0 offset:0xe00
	ds_read_b64_tr_b16 v[198:199], v0 offset:0x1600
	ds_read_b64_tr_b16 v[200:201], v0 offset:0x1e00
	v_exp_f32_e32 v96, v96
	v_exp_f32_e32 v97, v97
	v_add_f32_e32 v222, v72, v88
	v_add_f32_e32 v223, v73, v89
	v_add_f32_e32 v224, v224, v226
	v_add_f32_e32 v225, v225, v227
	v_exp_f32_e32 v98, v98
	v_exp_f32_e32 v99, v99
	v_add_f32_e32 v220, v74, v90
	v_add_f32_e32 v221, v75, v91
	v_add_f32_e32 v222, v222, v224
	v_add_f32_e32 v223, v223, v225
	s_waitcnt lgkmcnt(4)
	v_mfma_f32_32x32x16_bf16 v[52:67], v[170:173], v[186:189], v[52:67]
	v_mfma_f32_32x32x16_bf16 v[52:67], v[174:177], v[190:193], v[52:67]
	ds_read_b64_tr_b16 v[186:187], v0 offset:0x2000
	ds_read_b64_tr_b16 v[188:189], v0 offset:0x2800
	ds_read_b64_tr_b16 v[190:191], v0 offset:0x3000
	ds_read_b64_tr_b16 v[192:193], v0 offset:0x3800
	v_add_f32_e32 v218, v76, v92
	v_add_f32_e32 v219, v77, v93
	v_add_f32_e32 v220, v220, v222
	v_add_f32_e32 v221, v221, v223
	v_add_f32_e32 v216, v78, v94
	v_add_f32_e32 v217, v79, v95
	v_add_f32_e32 v218, v218, v220
	v_add_f32_e32 v219, v219, v221
	v_add_f32_e32 v214, v80, v96
	v_add_f32_e32 v215, v81, v97
	v_add_f32_e32 v216, v216, v218
	v_add_f32_e32 v217, v217, v219
	s_waitcnt lgkmcnt(4)
	v_mfma_f32_32x32x16_bf16 v[4:19], v[170:173], v[194:197], v[4:19]
	v_mfma_f32_32x32x16_bf16 v[4:19], v[174:177], v[198:201], v[4:19]
	ds_read_b64_tr_b16 v[194:195], v0 offset:0x2200
	ds_read_b64_tr_b16 v[196:197], v0 offset:0x2a00
	ds_read_b64_tr_b16 v[198:199], v0 offset:0x3200
	ds_read_b64_tr_b16 v[200:201], v0 offset:0x3a00
	v_add_f32_e32 v212, v82, v98
	v_add_f32_e32 v213, v83, v99
	v_add_f32_e32 v214, v214, v216
	v_add_f32_e32 v215, v215, v217
	s_nop 0
	v_add_f32_e32 v212, v212, v214
	v_add_f32_e32 v213, v213, v215
	s_nop 0
	v_pk_add_f32 v[212:213], v[212:213], v[212:213] op_sel:[0,1] op_sel_hi:[1,0]
	s_nop 0
	v_mov_b32_e32 v1, v212
	s_nop 1
	v_permlane32_swap_b32_e32 v212, v1
	v_add_f32_e32 v1, v212, v1
	v_fmac_f32_e32 v1, v138, v155
	v_mov_b32_e32 v138, v1
	v_cvt_pk_bf16_f32 v178, v84, v85
	v_cvt_pk_bf16_f32 v179, v86, v87
	v_cvt_pk_bf16_f32 v180, v88, v89
	v_cvt_pk_bf16_f32 v181, v90, v91
	v_cvt_pk_bf16_f32 v182, v92, v93
	v_cvt_pk_bf16_f32 v183, v94, v95
	v_cvt_pk_bf16_f32 v184, v96, v97
	v_cvt_pk_bf16_f32 v185, v98, v99
	v_permlane32_swap_b32_e32 v178, v180
	v_permlane32_swap_b32_e32 v179, v181
	v_permlane32_swap_b32_e32 v182, v184
	v_permlane32_swap_b32_e32 v183, v185
	s_nop 1
	s_waitcnt lgkmcnt(4)
	v_mfma_f32_32x32x16_bf16 v[20:35], v[178:181], v[186:189], v[20:35]
	v_mfma_f32_32x32x16_bf16 v[20:35], v[182:185], v[190:193], v[20:35]
	ds_read_b64_tr_b16 v[186:187], v0 offset:0x2400
	ds_read_b64_tr_b16 v[188:189], v0 offset:0x2c00
	ds_read_b64_tr_b16 v[190:191], v0 offset:0x3400
	ds_read_b64_tr_b16 v[192:193], v0 offset:0x3c00
	s_waitcnt lgkmcnt(4)
	v_mfma_f32_32x32x16_bf16 v[36:51], v[178:181], v[194:197], v[36:51]
	v_mfma_f32_32x32x16_bf16 v[36:51], v[182:185], v[198:201], v[36:51]
	ds_read_b64_tr_b16 v[194:195], v0 offset:0x2600
	ds_read_b64_tr_b16 v[196:197], v0 offset:0x2e00
	ds_read_b64_tr_b16 v[198:199], v0 offset:0x3600
	ds_read_b64_tr_b16 v[200:201], v0 offset:0x3e00
	s_waitcnt lgkmcnt(4)
	v_mfma_f32_32x32x16_bf16 v[52:67], v[178:181], v[186:189], v[52:67]
	v_mfma_f32_32x32x16_bf16 v[52:67], v[182:185], v[190:193], v[52:67]
	s_waitcnt lgkmcnt(0)
	v_mfma_f32_32x32x16_bf16 v[4:19], v[178:181], v[194:197], v[4:19]
	v_mfma_f32_32x32x16_bf16 v[4:19], v[182:185], v[198:201], v[4:19]

.LBB0_1869:
	ds_read_b64_tr_b16 v[186:187], v136 offset:0
	ds_read_b64_tr_b16 v[188:189], v136 offset:0x800
	ds_read_b64_tr_b16 v[190:191], v136 offset:0x1000
	ds_read_b64_tr_b16 v[192:193], v136 offset:0x1800
	ds_read_b64_tr_b16 v[194:195], v136 offset:0x200
	ds_read_b64_tr_b16 v[196:197], v136 offset:0xa00
	ds_read_b64_tr_b16 v[198:199], v136 offset:0x1200
	ds_read_b64_tr_b16 v[200:201], v136 offset:0x1a00
	v_cvt_pk_bf16_f32 v170, v68, v69
	v_cvt_pk_bf16_f32 v171, v70, v71
	v_cvt_pk_bf16_f32 v172, v72, v73
	v_cvt_pk_bf16_f32 v173, v74, v75
	v_cvt_pk_bf16_f32 v174, v76, v77
	v_cvt_pk_bf16_f32 v175, v78, v79
	v_cvt_pk_bf16_f32 v176, v80, v81
	v_cvt_pk_bf16_f32 v177, v82, v83
	v_permlane32_swap_b32_e32 v170, v172
	v_permlane32_swap_b32_e32 v171, v173
	v_permlane32_swap_b32_e32 v174, v176
	v_permlane32_swap_b32_e32 v175, v177
	v_exp_f32_e32 v84, v84
	v_exp_f32_e32 v85, v85
	v_exp_f32_e32 v86, v86
	v_exp_f32_e32 v87, v87
	v_exp_f32_e32 v88, v88
	v_exp_f32_e32 v89, v89
	s_waitcnt lgkmcnt(4)
	v_mfma_f32_32x32x16_bf16 v[20:35], v[170:173], v[186:189], v[20:35]
	v_mfma_f32_32x32x16_bf16 v[20:35], v[174:177], v[190:193], v[20:35]
	ds_read_b64_tr_b16 v[186:187], v136 offset:0x400
	ds_read_b64_tr_b16 v[188:189], v136 offset:0xc00
	ds_read_b64_tr_b16 v[190:191], v136 offset:0x1400
	ds_read_b64_tr_b16 v[192:193], v136 offset:0x1c00
	v_exp_f32_e32 v90, v90
	v_exp_f32_e32 v91, v91
	v_exp_f32_e32 v92, v92
	v_exp_f32_e32 v93, v93
	v_add_f32_e32 v226, v68, v84
	v_add_f32_e32 v227, v69, v85
	v_exp_f32_e32 v94, v94
	v_exp_f32_e32 v95, v95
	v_add_f32_e32 v224, v70, v86
	v_add_f32_e32 v225, v71, v87
	v_add_f32_e32 v226, 0, v226
	v_add_f32_e32 v227, 0, v227
	s_waitcnt lgkmcnt(4)
	v_mfma_f32_32x32x16_bf16 v[36:51], v[170:173], v[194:197], v[36:51]
	v_mfma_f32_32x32x16_bf16 v[36:51], v[174:177], v[198:201], v[36:51]
	ds_read_b64_tr_b16 v[194:195], v136 offset:0x600
	ds_read_b64_tr_b16 v[196:197], v136 offset:0xe00
	ds_read_b64_tr_b16 v[198:199], v136 offset:0x1600
	ds_read_b64_tr_b16 v[200:201], v136 offset:0x1e00
	v_exp_f32_e32 v96, v96
	v_exp_f32_e32 v97, v97
	v_add_f32_e32 v222, v72, v88
	v_add_f32_e32 v223, v73, v89
	v_add_f32_e32 v224, v224, v226
	v_add_f32_e32 v225, v225, v227
	v_exp_f32_e32 v98, v98
	v_exp_f32_e32 v99, v99
	v_add_f32_e32 v220, v74, v90
	v_add_f32_e32 v221, v75, v91
	v_add_f32_e32 v222, v222, v224
	v_add_f32_e32 v223, v223, v225
	s_waitcnt lgkmcnt(4)
	v_mfma_f32_32x32x16_bf16 v[52:67], v[170:173], v[186:189], v[52:67]
	v_mfma_f32_32x32x16_bf16 v[52:67], v[174:177], v[190:193], v[52:67]
	ds_read_b64_tr_b16 v[186:187], v136 offset:0x2000
	ds_read_b64_tr_b16 v[188:189], v136 offset:0x2800
	ds_read_b64_tr_b16 v[190:191], v136 offset:0x3000
	ds_read_b64_tr_b16 v[192:193], v136 offset:0x3800
	v_add_f32_e32 v218, v76, v92
	v_add_f32_e32 v219, v77, v93
	v_add_f32_e32 v220, v220, v222
	v_add_f32_e32 v221, v221, v223
	v_add_f32_e32 v216, v78, v94
	v_add_f32_e32 v217, v79, v95
	v_add_f32_e32 v218, v218, v220
	v_add_f32_e32 v219, v219, v221
	v_add_f32_e32 v214, v80, v96
	v_add_f32_e32 v215, v81, v97
	v_add_f32_e32 v216, v216, v218
	v_add_f32_e32 v217, v217, v219
	s_waitcnt lgkmcnt(4)
	v_mfma_f32_32x32x16_bf16 v[4:19], v[170:173], v[194:197], v[4:19]
	v_mfma_f32_32x32x16_bf16 v[4:19], v[174:177], v[198:201], v[4:19]
	ds_read_b64_tr_b16 v[194:195], v136 offset:0x2200
	ds_read_b64_tr_b16 v[196:197], v136 offset:0x2a00
	ds_read_b64_tr_b16 v[198:199], v136 offset:0x3200
	ds_read_b64_tr_b16 v[200:201], v136 offset:0x3a00
	v_add_f32_e32 v212, v82, v98
	v_add_f32_e32 v213, v83, v99
	v_add_f32_e32 v214, v214, v216
	v_add_f32_e32 v215, v215, v217
	s_nop 0
	v_add_f32_e32 v212, v212, v214
	v_add_f32_e32 v213, v213, v215
	s_nop 0
	v_pk_add_f32 v[212:213], v[212:213], v[212:213] op_sel:[0,1] op_sel_hi:[1,0]
	s_nop 0
	v_mov_b32_e32 v1, v212
	s_nop 1
	v_permlane32_swap_b32_e32 v212, v1
	v_add_f32_e32 v1, v212, v1
	v_fmac_f32_e32 v1, v138, v155
	v_mov_b32_e32 v138, v1
	v_cvt_pk_bf16_f32 v178, v84, v85
	v_cvt_pk_bf16_f32 v179, v86, v87
	v_cvt_pk_bf16_f32 v180, v88, v89
	v_cvt_pk_bf16_f32 v181, v90, v91
	v_cvt_pk_bf16_f32 v182, v92, v93
	v_cvt_pk_bf16_f32 v183, v94, v95
	v_cvt_pk_bf16_f32 v184, v96, v97
	v_cvt_pk_bf16_f32 v185, v98, v99
	v_permlane32_swap_b32_e32 v178, v180
	v_permlane32_swap_b32_e32 v179, v181
	v_permlane32_swap_b32_e32 v182, v184
	v_permlane32_swap_b32_e32 v183, v185
	s_nop 1
	s_waitcnt lgkmcnt(4)
	v_mfma_f32_32x32x16_bf16 v[20:35], v[178:181], v[186:189], v[20:35]
	v_mfma_f32_32x32x16_bf16 v[20:35], v[182:185], v[190:193], v[20:35]
	ds_read_b64_tr_b16 v[186:187], v136 offset:0x2400
	ds_read_b64_tr_b16 v[188:189], v136 offset:0x2c00
	ds_read_b64_tr_b16 v[190:191], v136 offset:0x3400
	ds_read_b64_tr_b16 v[192:193], v136 offset:0x3c00
	s_waitcnt lgkmcnt(4)
	v_mfma_f32_32x32x16_bf16 v[36:51], v[178:181], v[194:197], v[36:51]
	v_mfma_f32_32x32x16_bf16 v[36:51], v[182:185], v[198:201], v[36:51]
	ds_read_b64_tr_b16 v[194:195], v136 offset:0x2600
	ds_read_b64_tr_b16 v[196:197], v136 offset:0x2e00
	ds_read_b64_tr_b16 v[198:199], v136 offset:0x3600
	ds_read_b64_tr_b16 v[200:201], v136 offset:0x3e00
	s_waitcnt lgkmcnt(4)
	v_mfma_f32_32x32x16_bf16 v[52:67], v[178:181], v[186:189], v[52:67]
	v_mfma_f32_32x32x16_bf16 v[52:67], v[182:185], v[190:193], v[52:67]
	s_waitcnt lgkmcnt(0)
	v_mfma_f32_32x32x16_bf16 v[4:19], v[178:181], v[194:197], v[4:19]
	v_mfma_f32_32x32x16_bf16 v[4:19], v[182:185], v[198:201], v[4:19]
